# grid barrier: XCD leader posts the generation word before its own L1 invalidate (plus N2 batching, nt conversion hints)
# baseline (speedup 1.0000x reference)
; __device__ __forceinline__ unsigned xb_ld(unsigned* p)              { return __hip_atomic_load(p, __ATOMIC_RELAXED, __HIP_MEMORY_SCOPE_AGENT); }
; __device__ __forceinline__ unsigned xb_add(unsigned* p, unsigned v) { return __hip_atomic_fetch_add(p, v, __ATOMIC_RELAXED, __HIP_MEMORY_SCOPE_AGENT); }
; #define XB_SPIN(cond, bar) do { unsigned _sp = 0; while (cond) { __builtin_amdgcn_s_sleep(1); \
;     if ((++_sp & 255u) == 0u) { if (xb_ld(&(bar)[XB_TMO])) break; if (_sp > XB_SPIN_CAP) { atomicAdd(&(bar)[XB_TMO], 1u); break; } } } } while (0)
; __device__ __forceinline__ void xcd_barrier(const XcdBarrier& b) {
;     ...
;         const unsigned old = xb_add(&bar[XB_XSUB(b.x)], 1u);
;         const unsigned gen = old / nloc;
;         if (old + 1u == (gen + 1u) * nloc) {
;             __builtin_amdgcn_fence(__ATOMIC_RELEASE, "agent");
;             asm volatile("s_waitcnt vmcnt(0)" ::: "memory");
;             const unsigned og = xb_add(&bar[XB_TOP], 1u);
;             const unsigned tg = og / nx;
;             if (og + 1u == (tg + 1u) * nx) xb_add(&bar[XB_TOPGEN], 1u);
;             else XB_SPIN(xb_ld(&bar[XB_TOPGEN]) == tg, bar);
;             __builtin_amdgcn_fence(__ATOMIC_ACQUIRE, "agent");
;             xb_add(&bar[XB_XGEN(b.x)], 1u);
;             asm volatile("s_waitcnt vmcnt(0)" ::: "memory");
.LBB0_171:
	s_or_b64 exec, exec, s[4:5]
	s_mov_b64 s[4:5], exec
	v_mbcnt_lo_u32_b32 v1, s4, 0
	v_mbcnt_hi_u32_b32 v1, s5, v1
	v_cmp_eq_u32_e32 vcc, 0, v1
	s_waitcnt vmcnt(0)
	s_and_saveexec_b64 s[6:7], vcc
	s_cbranch_execz .LBB0_173
	s_bcnt1_i32_b64 s4, s[4:5]
	v_mov_b32_e32 v1, 0x2000
	v_mov_b32_e32 v2, s4
	global_atomic_add v1, v2, s[2:3] offset:1024
.LBB0_173:
	s_or_b64 exec, exec, s[6:7]
	buffer_inv sc1
	s_waitcnt vmcnt(0)

; __device__ __forceinline__ unsigned xb_ld(unsigned* p)              { return __hip_atomic_load(p, __ATOMIC_RELAXED, __HIP_MEMORY_SCOPE_AGENT); }
; __device__ __forceinline__ unsigned xb_add(unsigned* p, unsigned v) { return __hip_atomic_fetch_add(p, v, __ATOMIC_RELAXED, __HIP_MEMORY_SCOPE_AGENT); }
; #define XB_SPIN(cond, bar) do { unsigned _sp = 0; while (cond) { __builtin_amdgcn_s_sleep(1); \
;     if ((++_sp & 255u) == 0u) { if (xb_ld(&(bar)[XB_TMO])) break; if (_sp > XB_SPIN_CAP) { atomicAdd(&(bar)[XB_TMO], 1u); break; } } } } while (0)
; __device__ __forceinline__ void xcd_barrier(const XcdBarrier& b) {
;     ...
;             __builtin_amdgcn_fence(__ATOMIC_RELEASE, "agent");
;             asm volatile("s_waitcnt vmcnt(0)" ::: "memory");
;             const unsigned og = xb_add(&bar[XB_TOP], 1u);
;             const unsigned tg = og / nx;
;             if (og + 1u == (tg + 1u) * nx) xb_add(&bar[XB_TOPGEN], 1u);
;             else XB_SPIN(xb_ld(&bar[XB_TOPGEN]) == tg, bar);
;             __builtin_amdgcn_fence(__ATOMIC_ACQUIRE, "agent");
;             xb_add(&bar[XB_XGEN(b.x)], 1u);
;             asm volatile("s_waitcnt vmcnt(0)" ::: "memory");
;         } else {
;             XB_SPIN(xb_ld(&bar[XB_XGEN(b.x)]) == gen, bar);
;             __builtin_amdgcn_fence(__ATOMIC_ACQUIRE, "agent");
;             asm volatile("s_waitcnt vmcnt(0)" ::: "memory");
.LBB0_176:
	s_or_b64 exec, exec, s[4:5]
	buffer_inv sc1
	s_waitcnt vmcnt(0)

; __device__ __forceinline__ unsigned xb_ld(unsigned* p)              { return __hip_atomic_load(p, __ATOMIC_RELAXED, __HIP_MEMORY_SCOPE_AGENT); }
; __device__ __forceinline__ unsigned xb_add(unsigned* p, unsigned v) { return __hip_atomic_fetch_add(p, v, __ATOMIC_RELAXED, __HIP_MEMORY_SCOPE_AGENT); }
; #define XB_SPIN(cond, bar) do { unsigned _sp = 0; while (cond) { __builtin_amdgcn_s_sleep(1); \
;     if ((++_sp & 255u) == 0u) { if (xb_ld(&(bar)[XB_TMO])) break; if (_sp > XB_SPIN_CAP) { atomicAdd(&(bar)[XB_TMO], 1u); break; } } } } while (0)
; __device__ __forceinline__ void xcd_barrier(const XcdBarrier& b) {
;     ...
;         const unsigned old = xb_add(&bar[XB_XSUB(b.x)], 1u);
;         const unsigned gen = old / nloc;
;         if (old + 1u == (gen + 1u) * nloc) {
;             __builtin_amdgcn_fence(__ATOMIC_RELEASE, "agent");
;             asm volatile("s_waitcnt vmcnt(0)" ::: "memory");
;             const unsigned og = xb_add(&bar[XB_TOP], 1u);
;             const unsigned tg = og / nx;
;             if (og + 1u == (tg + 1u) * nx) xb_add(&bar[XB_TOPGEN], 1u);
;             else XB_SPIN(xb_ld(&bar[XB_TOPGEN]) == tg, bar);
;             __builtin_amdgcn_fence(__ATOMIC_ACQUIRE, "agent");
;             xb_add(&bar[XB_XGEN(b.x)], 1u);
;             asm volatile("s_waitcnt vmcnt(0)" ::: "memory");
.LBB0_453:
	s_or_b64 exec, exec, s[2:3]
	s_mov_b64 s[2:3], exec
	v_mbcnt_lo_u32_b32 v1, s2, 0
	v_mbcnt_hi_u32_b32 v1, s3, v1
	v_cmp_eq_u32_e32 vcc, 0, v1
	s_waitcnt vmcnt(0)
	s_and_saveexec_b64 s[4:5], vcc
	s_cbranch_execz .LBB0_455
	s_bcnt1_i32_b64 s2, s[2:3]
	v_mov_b32_e32 v1, s2
	v_readlane_b32 s2, v253, 26
	v_readlane_b32 s3, v253, 27
	s_nop 4
	global_atomic_add v191, v1, s[2:3]

; __device__ __forceinline__ unsigned xb_ld(unsigned* p)              { return __hip_atomic_load(p, __ATOMIC_RELAXED, __HIP_MEMORY_SCOPE_AGENT); }
; __device__ __forceinline__ unsigned xb_add(unsigned* p, unsigned v) { return __hip_atomic_fetch_add(p, v, __ATOMIC_RELAXED, __HIP_MEMORY_SCOPE_AGENT); }
; #define XB_SPIN(cond, bar) do { unsigned _sp = 0; while (cond) { __builtin_amdgcn_s_sleep(1); \
;     if ((++_sp & 255u) == 0u) { if (xb_ld(&(bar)[XB_TMO])) break; if (_sp > XB_SPIN_CAP) { atomicAdd(&(bar)[XB_TMO], 1u); break; } } } } while (0)
; __device__ __forceinline__ void xcd_barrier(const XcdBarrier& b) {
;     ...
;         const unsigned old = xb_add(&bar[XB_XSUB(b.x)], 1u);
;         const unsigned gen = old / nloc;
;         if (old + 1u == (gen + 1u) * nloc) {
;             __builtin_amdgcn_fence(__ATOMIC_RELEASE, "agent");
;             asm volatile("s_waitcnt vmcnt(0)" ::: "memory");
;             const unsigned og = xb_add(&bar[XB_TOP], 1u);
;             const unsigned tg = og / nx;
;             if (og + 1u == (tg + 1u) * nx) xb_add(&bar[XB_TOPGEN], 1u);
;             else XB_SPIN(xb_ld(&bar[XB_TOPGEN]) == tg, bar);
;             __builtin_amdgcn_fence(__ATOMIC_ACQUIRE, "agent");
;             xb_add(&bar[XB_XGEN(b.x)], 1u);
;             asm volatile("s_waitcnt vmcnt(0)" ::: "memory");
.LBB0_651:
	s_or_b64 exec, exec, s[4:5]
	s_mov_b64 s[4:5], exec
	v_mbcnt_lo_u32_b32 v1, s4, 0
	v_mbcnt_hi_u32_b32 v1, s5, v1
	v_cmp_eq_u32_e32 vcc, 0, v1
	s_waitcnt vmcnt(0)
	s_and_saveexec_b64 s[6:7], vcc
	s_cbranch_execz .LBB0_653
	s_bcnt1_i32_b64 s4, s[4:5]
	v_mov_b32_e32 v1, s4
	v_readlane_b32 s4, v253, 26
	v_readlane_b32 s5, v253, 27
	s_nop 4
	global_atomic_add v191, v1, s[4:5]

; __device__ __forceinline__ unsigned xb_ld(unsigned* p)              { return __hip_atomic_load(p, __ATOMIC_RELAXED, __HIP_MEMORY_SCOPE_AGENT); }
; __device__ __forceinline__ unsigned xb_add(unsigned* p, unsigned v) { return __hip_atomic_fetch_add(p, v, __ATOMIC_RELAXED, __HIP_MEMORY_SCOPE_AGENT); }
; #define XB_SPIN(cond, bar) do { unsigned _sp = 0; while (cond) { __builtin_amdgcn_s_sleep(1); \
;     if ((++_sp & 255u) == 0u) { if (xb_ld(&(bar)[XB_TMO])) break; if (_sp > XB_SPIN_CAP) { atomicAdd(&(bar)[XB_TMO], 1u); break; } } } } while (0)
; __device__ __forceinline__ void xcd_barrier(const XcdBarrier& b) {
;     ...
;         const unsigned old = xb_add(&bar[XB_XSUB(b.x)], 1u);
;         const unsigned gen = old / nloc;
;         if (old + 1u == (gen + 1u) * nloc) {
;             __builtin_amdgcn_fence(__ATOMIC_RELEASE, "agent");
;             asm volatile("s_waitcnt vmcnt(0)" ::: "memory");
;             const unsigned og = xb_add(&bar[XB_TOP], 1u);
;             const unsigned tg = og / nx;
;             if (og + 1u == (tg + 1u) * nx) xb_add(&bar[XB_TOPGEN], 1u);
;             else XB_SPIN(xb_ld(&bar[XB_TOPGEN]) == tg, bar);
;             __builtin_amdgcn_fence(__ATOMIC_ACQUIRE, "agent");
;             xb_add(&bar[XB_XGEN(b.x)], 1u);
;             asm volatile("s_waitcnt vmcnt(0)" ::: "memory");
.LBB0_1611:
	s_or_b64 exec, exec, s[2:3]
	s_mov_b64 s[2:3], exec
	v_mbcnt_lo_u32_b32 v1, s2, 0
	v_mbcnt_hi_u32_b32 v1, s3, v1
	v_cmp_eq_u32_e32 vcc, 0, v1
	s_waitcnt vmcnt(0)
	s_and_saveexec_b64 s[4:5], vcc
	s_cbranch_execnz .LBB0_1612
	s_getpc_b64 s[98:99]
